# phase 3: skip the structurally-zero bj=1 MFMA half of the w_in gate tile (pn==20); second half of the G^T units dealt one per workgroup
# baseline (speedup 1.0000x reference)
.LBB0_454:
	s_or_b64 exec, exec, s[34:35]
	s_add_i32 s11, s11, 2
	s_add_u32 s18, s28, 0x4000
	s_addc_u32 s20, s29, 0
	s_and_b64 s[14:15], s[30:31], exec
	s_cselect_b32 s64, s18, s46
	s_cselect_b32 s65, s20, s47
	s_cselect_b32 s35, s2, s63
	s_cselect_b32 s34, s1, s62
	s_add_u32 s30, s64, 0x8000
	s_addc_u32 s31, s65, 0
	s_add_u32 s38, s34, 0x8000
	s_addc_u32 s39, s35, 0
	s_add_i32 s14, 0, 0x10000
	v_add_u32_e32 v149, s14, v146
	s_add_i32 s18, 0, 0x14000
	ds_read_b128 v[132:135], v149
	ds_read_b128 v[136:139], v149 offset:1024
	ds_read_b128 v[150:153], v149 offset:2048
	ds_read_b128 v[154:157], v149 offset:3072
	v_add_u32_e32 v149, s18, v146
	ds_read_b128 v[158:161], v149
	ds_read_b128 v[162:165], v149 offset:1024
	ds_read_b128 v[166:169], v149 offset:2048
	ds_read_b128 v[170:173], v149 offset:3072
	s_add_i32 m0, s71, 0xc000
	ds_read_b128 v[174:177], v148
	ds_read_b128 v[178:181], v148 offset:1024
	ds_read_b128 v[182:185], v148 offset:2048
	ds_read_b128 v[186:189], v148 offset:3072
	ds_read_b128 v[194:197], v148 offset:4096
	ds_read_b128 v[198:201], v148 offset:5120
	ds_read_b128 v[202:205], v148 offset:6144
	ds_read_b128 v[206:209], v148 offset:7168
	s_nop 0
	global_load_lds_dwordx4 v142, s[28:29]
	s_add_i32 m0, s71, 0xe000
	s_nop 0
	global_load_lds_dwordx4 v144, s[28:29]
	s_waitcnt vmcnt(8)
	s_waitcnt lgkmcnt(0)
	s_setprio 1
	s_barrier
	s_waitcnt lgkmcnt(0)
	v_mfma_f32_16x16x32_bf16 v[66:69], v[132:135], v[174:177], v[66:69]
	v_mfma_f32_16x16x32_bf16 v[70:73], v[150:153], v[174:177], v[70:73]
	v_mfma_f32_16x16x32_bf16 v[58:61], v[132:135], v[182:185], v[58:61]
	v_mfma_f32_16x16x32_bf16 v[62:65], v[150:153], v[182:185], v[62:65]
	v_mfma_f32_16x16x32_bf16 v[50:53], v[132:135], v[194:197], v[50:53]
	v_mfma_f32_16x16x32_bf16 v[54:57], v[150:153], v[194:197], v[54:57]
	v_mfma_f32_16x16x32_bf16 v[42:45], v[132:135], v[202:205], v[42:45]
	v_mfma_f32_16x16x32_bf16 v[46:49], v[150:153], v[202:205], v[46:49]
	v_mfma_f32_16x16x32_bf16 v[66:69], v[136:139], v[178:181], v[66:69]
	v_mfma_f32_16x16x32_bf16 v[70:73], v[154:157], v[178:181], v[70:73]
	v_mfma_f32_16x16x32_bf16 v[58:61], v[136:139], v[186:189], v[58:61]
	v_mfma_f32_16x16x32_bf16 v[62:65], v[154:157], v[186:189], v[62:65]
	v_mfma_f32_16x16x32_bf16 v[50:53], v[136:139], v[198:201], v[50:53]
	v_mfma_f32_16x16x32_bf16 v[54:57], v[154:157], v[198:201], v[54:57]
	v_mfma_f32_16x16x32_bf16 v[42:45], v[136:139], v[206:209], v[42:45]
	v_mfma_f32_16x16x32_bf16 v[46:49], v[154:157], v[206:209], v[46:49]
	s_cmp_eq_u32 s0, 20
	s_cbranch_scc1 .Lgate_skip_0
	v_mfma_f32_16x16x32_bf16 v[126:129], v[158:161], v[174:177], v[126:129]
	v_mfma_f32_16x16x32_bf16 v[122:125], v[166:169], v[174:177], v[122:125]
	v_mfma_f32_16x16x32_bf16 v[118:121], v[158:161], v[182:185], v[118:121]
	v_mfma_f32_16x16x32_bf16 v[114:117], v[166:169], v[182:185], v[114:117]
	v_mfma_f32_16x16x32_bf16 v[110:113], v[158:161], v[194:197], v[110:113]
	v_mfma_f32_16x16x32_bf16 v[106:109], v[166:169], v[194:197], v[106:109]
	v_mfma_f32_16x16x32_bf16 v[94:97], v[158:161], v[202:205], v[94:97]
	v_mfma_f32_16x16x32_bf16 v[90:93], v[166:169], v[202:205], v[90:93]
	v_mfma_f32_16x16x32_bf16 v[126:129], v[162:165], v[178:181], v[126:129]
	v_mfma_f32_16x16x32_bf16 v[122:125], v[170:173], v[178:181], v[122:125]
	v_mfma_f32_16x16x32_bf16 v[118:121], v[162:165], v[186:189], v[118:121]
	v_mfma_f32_16x16x32_bf16 v[114:117], v[170:173], v[186:189], v[114:117]
	v_mfma_f32_16x16x32_bf16 v[110:113], v[162:165], v[198:201], v[110:113]
	v_mfma_f32_16x16x32_bf16 v[106:109], v[170:173], v[198:201], v[106:109]
	v_mfma_f32_16x16x32_bf16 v[94:97], v[162:165], v[206:209], v[94:97]
	v_mfma_f32_16x16x32_bf16 v[90:93], v[170:173], v[206:209], v[90:93]
.Lgate_skip_0:
	s_barrier
	s_setprio 0
	s_add_i32 s14, s14, s70
	s_mov_b32 m0, s14
	ds_read_b128 v[174:177], v148 offset:16384
	ds_read_b128 v[178:181], v148 offset:17408
	ds_read_b128 v[182:185], v148 offset:18432
	ds_read_b128 v[186:189], v148 offset:19456
	ds_read_b128 v[194:197], v148 offset:20480
	ds_read_b128 v[198:201], v148 offset:21504
	ds_read_b128 v[202:205], v148 offset:22528
	ds_read_b128 v[206:209], v148 offset:23552
	s_nop 0
	global_load_lds_dwordx4 v143, s[34:35]
	s_add_i32 m0, s14, 0x2000
	s_add_u32 s14, s34, 0x4000
	s_addc_u32 s15, s35, 0
	s_add_i32 s18, s18, s70
	s_nop 0
	global_load_lds_dwordx4 v145, s[34:35]
	s_mov_b32 m0, s18
	s_nop 0
	global_load_lds_dwordx4 v143, s[14:15]
	s_add_i32 m0, s18, 0x2000
	s_nop 0
	global_load_lds_dwordx4 v145, s[14:15]
	s_mov_b32 m0, s71
	s_nop 0
	global_load_lds_dwordx4 v142, s[64:65]
	s_mov_b32 m0, s72
	s_nop 0
	global_load_lds_dwordx4 v144, s[64:65]
	s_waitcnt vmcnt(8)
	s_waitcnt lgkmcnt(0)
	s_setprio 1
	s_barrier
	s_waitcnt lgkmcnt(0)
	v_mfma_f32_16x16x32_bf16 v[26:29], v[132:135], v[174:177], v[26:29]
	v_mfma_f32_16x16x32_bf16 v[30:33], v[150:153], v[174:177], v[30:33]
	v_mfma_f32_16x16x32_bf16 v[18:21], v[132:135], v[182:185], v[18:21]
	v_mfma_f32_16x16x32_bf16 v[22:25], v[150:153], v[182:185], v[22:25]
	v_mfma_f32_16x16x32_bf16 v[10:13], v[132:135], v[194:197], v[10:13]
	v_mfma_f32_16x16x32_bf16 v[14:17], v[150:153], v[194:197], v[14:17]
	v_mfma_f32_16x16x32_bf16 v[2:5], v[132:135], v[202:205], v[2:5]
	v_mfma_f32_16x16x32_bf16 v[6:9], v[150:153], v[202:205], v[6:9]
	v_mfma_f32_16x16x32_bf16 v[26:29], v[136:139], v[178:181], v[26:29]
	v_mfma_f32_16x16x32_bf16 v[30:33], v[154:157], v[178:181], v[30:33]
	v_mfma_f32_16x16x32_bf16 v[18:21], v[136:139], v[186:189], v[18:21]
	v_mfma_f32_16x16x32_bf16 v[22:25], v[154:157], v[186:189], v[22:25]
	v_mfma_f32_16x16x32_bf16 v[10:13], v[136:139], v[198:201], v[10:13]
	v_mfma_f32_16x16x32_bf16 v[14:17], v[154:157], v[198:201], v[14:17]
	v_mfma_f32_16x16x32_bf16 v[2:5], v[136:139], v[206:209], v[2:5]
	v_mfma_f32_16x16x32_bf16 v[6:9], v[154:157], v[206:209], v[6:9]
	s_cmp_eq_u32 s0, 20
	s_cbranch_scc1 .Lgate_skip_1
	v_mfma_f32_16x16x32_bf16 v[102:105], v[158:161], v[174:177], v[102:105]
	v_mfma_f32_16x16x32_bf16 v[98:101], v[166:169], v[174:177], v[98:101]
	v_mfma_f32_16x16x32_bf16 v[82:85], v[158:161], v[182:185], v[82:85]
	v_mfma_f32_16x16x32_bf16 v[86:89], v[166:169], v[182:185], v[86:89]
	v_mfma_f32_16x16x32_bf16 v[78:81], v[158:161], v[194:197], v[78:81]
	v_mfma_f32_16x16x32_bf16 v[74:77], v[166:169], v[194:197], v[74:77]
	v_mfma_f32_16x16x32_bf16 v[34:37], v[158:161], v[202:205], v[34:37]
	v_mfma_f32_16x16x32_bf16 v[38:41], v[166:169], v[202:205], v[38:41]
	v_mfma_f32_16x16x32_bf16 v[102:105], v[162:165], v[178:181], v[102:105]
	v_mfma_f32_16x16x32_bf16 v[98:101], v[170:173], v[178:181], v[98:101]
	v_mfma_f32_16x16x32_bf16 v[82:85], v[162:165], v[186:189], v[82:85]
	v_mfma_f32_16x16x32_bf16 v[86:89], v[170:173], v[186:189], v[86:89]
	v_mfma_f32_16x16x32_bf16 v[78:81], v[162:165], v[198:201], v[78:81]
	v_mfma_f32_16x16x32_bf16 v[74:77], v[170:173], v[198:201], v[74:77]
	v_mfma_f32_16x16x32_bf16 v[34:37], v[162:165], v[206:209], v[34:37]
	v_mfma_f32_16x16x32_bf16 v[38:41], v[170:173], v[206:209], v[38:41]
.Lgate_skip_1:
	s_barrier
	s_setprio 0
	s_add_i32 s18, 0, 0x18000
	v_add_u32_e32 v149, s18, v146
	s_add_i32 s20, 0, 0x1c000
	ds_read_b128 v[132:135], v149
	ds_read_b128 v[136:139], v149 offset:1024
	ds_read_b128 v[150:153], v149 offset:2048
	ds_read_b128 v[154:157], v149 offset:3072
	v_add_u32_e32 v149, s20, v146
	ds_read_b128 v[158:161], v149
	ds_read_b128 v[162:165], v149 offset:1024
	ds_read_b128 v[166:169], v149 offset:2048
	ds_read_b128 v[170:173], v149 offset:3072
	s_add_u32 s14, s64, 0x4000
	s_addc_u32 s15, s65, 0
	s_mov_b32 m0, s73
	ds_read_b128 v[174:177], v148 offset:32768
	ds_read_b128 v[178:181], v148 offset:33792
	ds_read_b128 v[182:185], v148 offset:34816
	ds_read_b128 v[186:189], v148 offset:35840
	ds_read_b128 v[194:197], v148 offset:36864
	ds_read_b128 v[198:201], v148 offset:37888
	ds_read_b128 v[202:205], v148 offset:38912
	ds_read_b128 v[206:209], v148 offset:39936
	s_nop 0
	global_load_lds_dwordx4 v142, s[14:15]
	s_mov_b32 m0, s74
	s_nop 0
	global_load_lds_dwordx4 v144, s[14:15]
	s_waitcnt vmcnt(8)
	s_waitcnt lgkmcnt(0)
	s_setprio 1
	s_barrier
	s_waitcnt lgkmcnt(0)
	v_mfma_f32_16x16x32_bf16 v[66:69], v[132:135], v[174:177], v[66:69]
	v_mfma_f32_16x16x32_bf16 v[70:73], v[150:153], v[174:177], v[70:73]
	v_mfma_f32_16x16x32_bf16 v[58:61], v[132:135], v[182:185], v[58:61]
	v_mfma_f32_16x16x32_bf16 v[62:65], v[150:153], v[182:185], v[62:65]
	v_mfma_f32_16x16x32_bf16 v[50:53], v[132:135], v[194:197], v[50:53]
	v_mfma_f32_16x16x32_bf16 v[54:57], v[150:153], v[194:197], v[54:57]
	v_mfma_f32_16x16x32_bf16 v[42:45], v[132:135], v[202:205], v[42:45]
	v_mfma_f32_16x16x32_bf16 v[46:49], v[150:153], v[202:205], v[46:49]
	v_mfma_f32_16x16x32_bf16 v[66:69], v[136:139], v[178:181], v[66:69]
	v_mfma_f32_16x16x32_bf16 v[70:73], v[154:157], v[178:181], v[70:73]
	v_mfma_f32_16x16x32_bf16 v[58:61], v[136:139], v[186:189], v[58:61]
	v_mfma_f32_16x16x32_bf16 v[62:65], v[154:157], v[186:189], v[62:65]
	v_mfma_f32_16x16x32_bf16 v[50:53], v[136:139], v[198:201], v[50:53]
	v_mfma_f32_16x16x32_bf16 v[54:57], v[154:157], v[198:201], v[54:57]
	v_mfma_f32_16x16x32_bf16 v[42:45], v[136:139], v[206:209], v[42:45]
	v_mfma_f32_16x16x32_bf16 v[46:49], v[154:157], v[206:209], v[46:49]
	s_cmp_eq_u32 s0, 20
	s_cbranch_scc1 .Lgate_skip_2
	v_mfma_f32_16x16x32_bf16 v[126:129], v[158:161], v[174:177], v[126:129]
	v_mfma_f32_16x16x32_bf16 v[122:125], v[166:169], v[174:177], v[122:125]
	v_mfma_f32_16x16x32_bf16 v[118:121], v[158:161], v[182:185], v[118:121]
	v_mfma_f32_16x16x32_bf16 v[114:117], v[166:169], v[182:185], v[114:117]
	v_mfma_f32_16x16x32_bf16 v[110:113], v[158:161], v[194:197], v[110:113]
	v_mfma_f32_16x16x32_bf16 v[106:109], v[166:169], v[194:197], v[106:109]
	v_mfma_f32_16x16x32_bf16 v[94:97], v[158:161], v[202:205], v[94:97]
	v_mfma_f32_16x16x32_bf16 v[90:93], v[166:169], v[202:205], v[90:93]
	v_mfma_f32_16x16x32_bf16 v[126:129], v[162:165], v[178:181], v[126:129]
	v_mfma_f32_16x16x32_bf16 v[122:125], v[170:173], v[178:181], v[122:125]
	v_mfma_f32_16x16x32_bf16 v[118:121], v[162:165], v[186:189], v[118:121]
	v_mfma_f32_16x16x32_bf16 v[114:117], v[170:173], v[186:189], v[114:117]
	v_mfma_f32_16x16x32_bf16 v[110:113], v[162:165], v[198:201], v[110:113]
	v_mfma_f32_16x16x32_bf16 v[106:109], v[170:173], v[198:201], v[106:109]
	v_mfma_f32_16x16x32_bf16 v[94:97], v[162:165], v[206:209], v[94:97]
	v_mfma_f32_16x16x32_bf16 v[90:93], v[170:173], v[206:209], v[90:93]
.Lgate_skip_2:
	s_barrier
	s_setprio 0
	s_add_i32 s14, s18, s70
	s_mov_b32 m0, s14
	ds_read_b128 v[174:177], v148 offset:49152
	ds_read_b128 v[178:181], v148 offset:50176
	ds_read_b128 v[182:185], v148 offset:51200
	ds_read_b128 v[186:189], v148 offset:52224
	ds_read_b128 v[194:197], v148 offset:53248
	ds_read_b128 v[198:201], v148 offset:54272
	ds_read_b128 v[202:205], v148 offset:55296
	ds_read_b128 v[206:209], v148 offset:56320
	s_nop 0
	global_load_lds_dwordx4 v143, s[38:39]
	s_add_i32 m0, s14, 0x2000
	s_add_u32 s14, s34, 0xc000
	s_addc_u32 s15, s35, 0
	s_add_i32 s18, s20, s70
	s_nop 0
	global_load_lds_dwordx4 v145, s[38:39]
	s_mov_b32 m0, s18
	s_nop 0
	global_load_lds_dwordx4 v143, s[14:15]
	s_add_i32 m0, s18, 0x2000
	s_nop 0
	global_load_lds_dwordx4 v145, s[14:15]
	s_mov_b32 m0, s81
	s_nop 0
	global_load_lds_dwordx4 v142, s[30:31]
	s_mov_b32 m0, s82
	s_nop 0
	global_load_lds_dwordx4 v144, s[30:31]
	s_waitcnt vmcnt(8)
	s_waitcnt lgkmcnt(0)
	s_setprio 1
	s_barrier
	s_waitcnt lgkmcnt(0)
	v_mfma_f32_16x16x32_bf16 v[26:29], v[132:135], v[174:177], v[26:29]
	v_mfma_f32_16x16x32_bf16 v[30:33], v[150:153], v[174:177], v[30:33]
	v_mfma_f32_16x16x32_bf16 v[18:21], v[132:135], v[182:185], v[18:21]
	v_mfma_f32_16x16x32_bf16 v[22:25], v[150:153], v[182:185], v[22:25]
	v_mfma_f32_16x16x32_bf16 v[10:13], v[132:135], v[194:197], v[10:13]
	v_mfma_f32_16x16x32_bf16 v[14:17], v[150:153], v[194:197], v[14:17]
	v_mfma_f32_16x16x32_bf16 v[2:5], v[132:135], v[202:205], v[2:5]
	v_mfma_f32_16x16x32_bf16 v[6:9], v[150:153], v[202:205], v[6:9]
	v_mfma_f32_16x16x32_bf16 v[26:29], v[136:139], v[178:181], v[26:29]
	v_mfma_f32_16x16x32_bf16 v[30:33], v[154:157], v[178:181], v[30:33]
	v_mfma_f32_16x16x32_bf16 v[18:21], v[136:139], v[186:189], v[18:21]
	v_mfma_f32_16x16x32_bf16 v[22:25], v[154:157], v[186:189], v[22:25]
	v_mfma_f32_16x16x32_bf16 v[10:13], v[136:139], v[198:201], v[10:13]
	v_mfma_f32_16x16x32_bf16 v[14:17], v[154:157], v[198:201], v[14:17]
	v_mfma_f32_16x16x32_bf16 v[2:5], v[136:139], v[206:209], v[2:5]
	v_mfma_f32_16x16x32_bf16 v[6:9], v[154:157], v[206:209], v[6:9]
	s_cmp_eq_u32 s0, 20
	s_cbranch_scc1 .Lgate_skip_3
	v_mfma_f32_16x16x32_bf16 v[102:105], v[158:161], v[174:177], v[102:105]
	v_mfma_f32_16x16x32_bf16 v[98:101], v[166:169], v[174:177], v[98:101]
	v_mfma_f32_16x16x32_bf16 v[82:85], v[158:161], v[182:185], v[82:85]
	v_mfma_f32_16x16x32_bf16 v[86:89], v[166:169], v[182:185], v[86:89]
	v_mfma_f32_16x16x32_bf16 v[78:81], v[158:161], v[194:197], v[78:81]
	v_mfma_f32_16x16x32_bf16 v[74:77], v[166:169], v[194:197], v[74:77]
	v_mfma_f32_16x16x32_bf16 v[34:37], v[158:161], v[202:205], v[34:37]
	v_mfma_f32_16x16x32_bf16 v[38:41], v[166:169], v[202:205], v[38:41]
	v_mfma_f32_16x16x32_bf16 v[102:105], v[162:165], v[178:181], v[102:105]
	v_mfma_f32_16x16x32_bf16 v[98:101], v[170:173], v[178:181], v[98:101]
	v_mfma_f32_16x16x32_bf16 v[82:85], v[162:165], v[186:189], v[82:85]
	v_mfma_f32_16x16x32_bf16 v[86:89], v[170:173], v[186:189], v[86:89]
	v_mfma_f32_16x16x32_bf16 v[78:81], v[162:165], v[198:201], v[78:81]
	v_mfma_f32_16x16x32_bf16 v[74:77], v[170:173], v[198:201], v[74:77]
	v_mfma_f32_16x16x32_bf16 v[34:37], v[162:165], v[206:209], v[34:37]
	v_mfma_f32_16x16x32_bf16 v[38:41], v[170:173], v[206:209], v[38:41]
.Lgate_skip_3:
	s_barrier
	s_setprio 0
	s_add_u32 s1, s1, 0x10000
	s_addc_u32 s2, s2, 0
	s_add_u32 s28, s28, 0x10000
	s_addc_u32 s29, s29, 0
	s_cmp_ge_i32 s11, s78
	s_cbranch_scc1 .LBB0_457

.LBB0_474:
	s_mov_b32 s21, 0
	s_andn2_b64 vcc, exec, s[28:29]
	s_mov_b32 s60, s3
	s_cbranch_vccnz .LBB0_476
	s_movk_i32 s94, 0x100
	s_and_b64 s[28:29], s[36:37], exec
	v_readlane_b32 s11, v251, 0
	v_readlane_b32 s21, v252, 49
	s_mov_b32 s60, s94
	s_cselect_b32 s21, 0, 0x100
